# speedup vs baseline: 1.1193x; 1.1193x over previous
.Lpoll_issued:
	s_add_i32 s25, s24, 1
	v_cmp_eq_u32_e64 s[2:3], s16, v193
	s_lshl_b32 s12, s16, 10
	v_or_b32_e32 v222, s12, v198
	v_lshlrev_b32_e32 v222, 4, v222
	ds_read_b128 v[130:133], v222
	ds_read_b128 v[126:129], v222 offset:1024
	ds_read_b128 v[122:125], v222 offset:2048
	ds_read_b128 v[118:121], v222 offset:3072
	ds_read_b128 v[114:117], v222 offset:4096
	ds_read_b128 v[110:113], v222 offset:5120
	ds_read_b128 v[194:197], v222 offset:6144
	ds_read_b128 v[202:205], v222 offset:7168
	ds_read_b128 v[162:165], v222 offset:8192
	ds_read_b128 v[158:161], v222 offset:9216
	ds_read_b128 v[154:157], v222 offset:10240
	ds_read_b128 v[150:153], v222 offset:11264
	ds_read_b128 v[146:149], v222 offset:12288
	ds_read_b128 v[142:145], v222 offset:13312
	ds_read_b128 v[138:141], v222 offset:14336
	ds_read_b128 v[134:137], v222 offset:15360
	s_add_i32 s12, s24, -1
	s_bfe_i32 s13, s12, 0x10001
	s_and_b32 s30, s13, 0x40004000
	s_lshl_b32 s34, s24, 13
	s_and_b32 s34, s34, 0x4000
	v_mov_b32_e32 v3, 0xbfffbfff
	v_cndmask_b32_e64 v167, 0, v3, s[2:3]
	s_lshl_b32 s14, s24, 10
	v_lshl_add_u64 v[178:179], s[14:15], 2, v[96:97]
	v_bitop3_b32 v2, s25, v193, 1 bitop3:0x6c
	v_add_u32_e32 v2, s25, v2
	v_min_i32_e32 v2, 0x1ff, v2
	s_and_b32 s12, s25, 1
	v_lshlrev_b32_e32 v200, 11, v2
	v_lshl_add_u64 v[2:3], v[210:211], 0, v[200:201]
	s_lshl_b32 s14, s12, 8
	v_lshl_add_u64 v[4:5], v[2:3], 0, s[14:15]
	s_lshl_b32 s17, s16, 14
	s_bitset1_b32 s17, 17
	s_add_i32 s26, s17, s21
	v_lshlrev_b32_e32 v2, 4, v217
	v_add3_u32 v174, s26, v2, v103
	s_lshl_b32 s12, s20, 4
	s_add_i32 s12, s12, s17
	v_add3_u32 v175, s12, v105, v103
	v_lshl_add_u32 v176, s16, 17, v106
	s_xor_b32 s12, s24, s22
	s_and_b32 s31, s12, 15
	s_and_b32 s12, s24, 0x1f0
	s_add_i32 s12, s23, s12
	s_min_i32 s12, s12, 0x1ff
	s_ashr_i32 s13, s12, 31
	s_lshl_b64 s[12:13], s[12:13], 11
	v_lshl_add_u64 v[172:173], v[0:1], 0, s[12:13]
	v_cndmask_b32_e64 v18, 0, v18, s[2:3]
	v_cndmask_b32_e64 v19, 0, v19, s[2:3]
	v_cndmask_b32_e64 v20, 0, v20, s[2:3]
	v_cndmask_b32_e64 v21, 0, v21, s[2:3]
	v_cndmask_b32_e64 v22, 0, v22, s[2:3]
	v_cndmask_b32_e64 v23, 0, v23, s[2:3]
	v_cndmask_b32_e64 v24, 0, v24, s[2:3]
	v_cndmask_b32_e64 v25, 0, v25, s[2:3]
	v_cndmask_b32_e64 v26, 0, v26, s[2:3]
	v_cndmask_b32_e64 v27, 0, v27, s[2:3]
	v_cndmask_b32_e64 v28, 0, v28, s[2:3]
	v_cndmask_b32_e64 v29, 0, v29, s[2:3]
	v_cndmask_b32_e64 v30, 0, v30, s[2:3]
	v_cndmask_b32_e64 v31, 0, v31, s[2:3]
	v_cndmask_b32_e64 v32, 0, v32, s[2:3]
	v_cndmask_b32_e64 v33, 0, v33, s[2:3]
	v_cndmask_b32_e64 v34, 0, v34, s[2:3]
	v_cndmask_b32_e64 v35, 0, v35, s[2:3]
	v_cndmask_b32_e64 v36, 0, v36, s[2:3]
	v_cndmask_b32_e64 v37, 0, v37, s[2:3]
	s_waitcnt vmcnt(8)
	v_cvt_pk_f16_f32 v180, v46, v47
	v_cvt_pk_f16_f32 v181, v48, v49
	v_cvt_pk_f16_f32 v182, v50, v51
	v_cvt_pk_f16_f32 v183, v52, v53
	v_cvt_pk_f16_f32 v218, v38, v39
	v_cvt_pk_f16_f32 v219, v40, v41
	v_cvt_pk_f16_f32 v220, v42, v43
	v_cvt_pk_f16_f32 v221, v44, v45
	s_mov_b32 s17, 0
	s_waitcnt lgkmcnt(8)
	v_mfma_f32_16x16x32_f16 v[6:9], v[130:133], v[180:183], v[6:9]
	v_mfma_f32_16x16x32_f16 v[10:13], v[126:129], v[180:183], v[10:13]
	v_mfma_f32_16x16x32_f16 v[14:17], v[122:125], v[180:183], v[14:17]
	v_mfma_f32_16x16x32_f16 v[18:21], v[118:121], v[180:183], v[18:21]
	v_mfma_f32_16x16x32_f16 v[22:25], v[114:117], v[180:183], v[22:25]
	v_mfma_f32_16x16x32_f16 v[26:29], v[110:113], v[180:183], v[26:29]
	v_mfma_f32_16x16x32_f16 v[30:33], v[194:197], v[180:183], v[30:33]
	v_mfma_f32_16x16x32_f16 v[34:37], v[202:205], v[180:183], v[34:37]
	s_waitcnt lgkmcnt(0)
	v_mfma_f32_16x16x32_f16 v[6:9], v[162:165], v[218:221], v[6:9]
	v_mfma_f32_16x16x32_f16 v[10:13], v[158:161], v[218:221], v[10:13]
	v_mfma_f32_16x16x32_f16 v[14:17], v[154:157], v[218:221], v[14:17]
	s_waitcnt vmcnt(7)
	v_mfma_f32_16x16x32_f16 v[18:21], v[150:153], v[218:221], v[18:21]
	v_bitop3_b32 v168, v62, v63, s30 bitop3:0x7e
	v_bitop3_b32 v169, v64, v65, s30 bitop3:0x7e
	v_mfma_f32_16x16x32_f16 v[22:25], v[146:149], v[218:221], v[22:25]
	v_bitop3_b32 v168, v168, v169, s18 bitop3:0xa8
	v_cmp_ne_u32_e32 vcc, 0, v168
	v_mfma_f32_16x16x32_f16 v[26:29], v[142:145], v[218:221], v[26:29]
	v_and_b32_e32 v62, v62, v167
	v_and_b32_e32 v63, v63, v167
	v_mfma_f32_16x16x32_f16 v[30:33], v[138:141], v[218:221], v[30:33]
	v_and_b32_e32 v64, v64, v167
	v_and_b32_e32 v65, v65, v167
	v_mfma_f32_16x16x32_f16 v[34:37], v[134:137], v[218:221], v[34:37]
	s_cmp_eq_u32 s24, 0
	s_cbranch_scc1 .Lall_chunks_done
	s_cbranch_vccnz .Lrestart0
.Lfast0:
	v_mfma_f32_16x16x32_f16 v[6:9], a[0:3], v[62:65], v[6:9]
	v_mfma_f32_16x16x32_f16 v[10:13], a[32:35], v[62:65], v[10:13]
	v_mfma_f32_16x16x32_f16 v[14:17], a[64:67], v[62:65], v[14:17]
	s_waitcnt vmcnt(6)
	v_mfma_f32_16x16x32_f16 v[18:21], a[96:99], v[62:65], v[18:21]
	v_bitop3_b32 v168, v66, v67, s30 bitop3:0x7e
	v_bitop3_b32 v169, v68, v69, s30 bitop3:0x7e
	v_mfma_f32_16x16x32_f16 v[22:25], a[128:131], v[62:65], v[22:25]
	v_bitop3_b32 v168, v168, v169, s18 bitop3:0xa8
	v_cmp_ne_u32_e32 vcc, 0, v168
	v_mfma_f32_16x16x32_f16 v[26:29], a[160:163], v[62:65], v[26:29]
	v_and_b32_e32 v66, v66, v167
	v_and_b32_e32 v67, v67, v167
	v_mfma_f32_16x16x32_f16 v[30:33], a[192:195], v[62:65], v[30:33]
	v_and_b32_e32 v68, v68, v167
	v_and_b32_e32 v69, v69, v167
	v_mfma_f32_16x16x32_f16 v[34:37], a[224:227], v[62:65], v[34:37]
	s_cbranch_vccnz .Lrestart1
.Lfast1:
	v_mfma_f32_16x16x32_f16 v[6:9], a[4:7], v[66:69], v[6:9]
	v_mfma_f32_16x16x32_f16 v[10:13], a[36:39], v[66:69], v[10:13]
	v_mfma_f32_16x16x32_f16 v[14:17], a[68:71], v[66:69], v[14:17]
	s_waitcnt vmcnt(5)
	v_mfma_f32_16x16x32_f16 v[18:21], a[100:103], v[66:69], v[18:21]
	v_bitop3_b32 v168, v70, v71, s30 bitop3:0x7e
	v_bitop3_b32 v169, v72, v73, s30 bitop3:0x7e
	v_mfma_f32_16x16x32_f16 v[22:25], a[132:135], v[66:69], v[22:25]
	v_bitop3_b32 v168, v168, v169, s18 bitop3:0xa8
	v_cmp_ne_u32_e32 vcc, 0, v168
	v_mfma_f32_16x16x32_f16 v[26:29], a[164:167], v[66:69], v[26:29]
	v_and_b32_e32 v70, v70, v167
	v_and_b32_e32 v71, v71, v167
	v_mfma_f32_16x16x32_f16 v[30:33], a[196:199], v[66:69], v[30:33]
	v_and_b32_e32 v72, v72, v167
	v_and_b32_e32 v73, v73, v167
	v_mfma_f32_16x16x32_f16 v[34:37], a[228:231], v[66:69], v[34:37]
	s_cbranch_vccnz .Lrestart2
.Lfast2:
	v_mfma_f32_16x16x32_f16 v[6:9], a[8:11], v[70:73], v[6:9]
	v_mfma_f32_16x16x32_f16 v[10:13], a[40:43], v[70:73], v[10:13]
	v_mfma_f32_16x16x32_f16 v[14:17], a[72:75], v[70:73], v[14:17]
	s_waitcnt vmcnt(4)
	v_mfma_f32_16x16x32_f16 v[18:21], a[104:107], v[70:73], v[18:21]
	v_bitop3_b32 v168, v74, v75, s30 bitop3:0x7e
	v_bitop3_b32 v169, v76, v77, s30 bitop3:0x7e
	v_mfma_f32_16x16x32_f16 v[22:25], a[136:139], v[70:73], v[22:25]
	v_bitop3_b32 v168, v168, v169, s18 bitop3:0xa8
	v_cmp_ne_u32_e32 vcc, 0, v168
	v_mfma_f32_16x16x32_f16 v[26:29], a[168:171], v[70:73], v[26:29]
	v_and_b32_e32 v74, v74, v167
	v_and_b32_e32 v75, v75, v167
	v_mfma_f32_16x16x32_f16 v[30:33], a[200:203], v[70:73], v[30:33]
	v_and_b32_e32 v76, v76, v167
	v_and_b32_e32 v77, v77, v167
	v_mfma_f32_16x16x32_f16 v[34:37], a[232:235], v[70:73], v[34:37]
	s_cbranch_vccnz .Lrestart3
.Lfast3:
	v_mfma_f32_16x16x32_f16 v[6:9], a[12:15], v[74:77], v[6:9]
	v_mfma_f32_16x16x32_f16 v[10:13], a[44:47], v[74:77], v[10:13]
	v_mfma_f32_16x16x32_f16 v[14:17], a[76:79], v[74:77], v[14:17]
	s_waitcnt vmcnt(3)
	v_mfma_f32_16x16x32_f16 v[18:21], a[108:111], v[74:77], v[18:21]
	v_bitop3_b32 v168, v78, v79, s30 bitop3:0x7e
	v_bitop3_b32 v169, v80, v81, s30 bitop3:0x7e
	v_mfma_f32_16x16x32_f16 v[22:25], a[140:143], v[74:77], v[22:25]
	v_bitop3_b32 v168, v168, v169, s18 bitop3:0xa8
	v_cmp_ne_u32_e32 vcc, 0, v168
	v_mfma_f32_16x16x32_f16 v[26:29], a[172:175], v[74:77], v[26:29]
	v_and_b32_e32 v78, v78, v167
	v_and_b32_e32 v79, v79, v167
	v_mfma_f32_16x16x32_f16 v[30:33], a[204:207], v[74:77], v[30:33]
	v_and_b32_e32 v80, v80, v167
	v_and_b32_e32 v81, v81, v167
	v_mfma_f32_16x16x32_f16 v[34:37], a[236:239], v[74:77], v[34:37]
	s_cbranch_vccnz .Lrestart4
.Lfast4:
	v_mfma_f32_16x16x32_f16 v[6:9], a[16:19], v[78:81], v[6:9]
	v_mfma_f32_16x16x32_f16 v[10:13], a[48:51], v[78:81], v[10:13]
	v_mfma_f32_16x16x32_f16 v[14:17], a[80:83], v[78:81], v[14:17]
	s_waitcnt vmcnt(2)
	v_mfma_f32_16x16x32_f16 v[18:21], a[112:115], v[78:81], v[18:21]
	v_bitop3_b32 v168, v82, v83, s30 bitop3:0x7e
	v_bitop3_b32 v169, v84, v85, s30 bitop3:0x7e
	v_mfma_f32_16x16x32_f16 v[22:25], a[144:147], v[78:81], v[22:25]
	v_bitop3_b32 v168, v168, v169, s18 bitop3:0xa8
	v_cmp_ne_u32_e32 vcc, 0, v168
	v_mfma_f32_16x16x32_f16 v[26:29], a[176:179], v[78:81], v[26:29]
	v_and_b32_e32 v82, v82, v167
	v_and_b32_e32 v83, v83, v167
	v_mfma_f32_16x16x32_f16 v[30:33], a[208:211], v[78:81], v[30:33]
	v_and_b32_e32 v84, v84, v167
	v_and_b32_e32 v85, v85, v167
	v_mfma_f32_16x16x32_f16 v[34:37], a[240:243], v[78:81], v[34:37]
	s_cbranch_vccnz .Lrestart5
.Lfast5:
	v_mfma_f32_16x16x32_f16 v[6:9], a[20:23], v[82:85], v[6:9]
	v_mfma_f32_16x16x32_f16 v[10:13], a[52:55], v[82:85], v[10:13]
	v_mfma_f32_16x16x32_f16 v[14:17], a[84:87], v[82:85], v[14:17]
	s_waitcnt vmcnt(1)
	v_mfma_f32_16x16x32_f16 v[18:21], a[116:119], v[82:85], v[18:21]
	v_bitop3_b32 v168, v86, v87, s30 bitop3:0x7e
	v_bitop3_b32 v169, v88, v89, s30 bitop3:0x7e
	v_mfma_f32_16x16x32_f16 v[22:25], a[148:151], v[82:85], v[22:25]
	v_bitop3_b32 v168, v168, v169, s18 bitop3:0xa8
	v_cmp_ne_u32_e32 vcc, 0, v168
	v_mfma_f32_16x16x32_f16 v[26:29], a[180:183], v[82:85], v[26:29]
	v_and_b32_e32 v86, v86, v167
	v_and_b32_e32 v87, v87, v167
	v_mfma_f32_16x16x32_f16 v[30:33], a[212:215], v[82:85], v[30:33]
	v_and_b32_e32 v88, v88, v167
	v_and_b32_e32 v89, v89, v167
	v_mfma_f32_16x16x32_f16 v[34:37], a[244:247], v[82:85], v[34:37]
	s_cbranch_vccnz .Lrestart6
.Lfast6:
	v_mfma_f32_16x16x32_f16 v[6:9], a[24:27], v[86:89], v[6:9]
	v_mfma_f32_16x16x32_f16 v[10:13], a[56:59], v[86:89], v[10:13]
	v_mfma_f32_16x16x32_f16 v[14:17], a[88:91], v[86:89], v[14:17]
	s_waitcnt vmcnt(0)
	v_mfma_f32_16x16x32_f16 v[18:21], a[120:123], v[86:89], v[18:21]
	v_bitop3_b32 v168, v90, v91, s30 bitop3:0x7e
	v_bitop3_b32 v169, v92, v93, s30 bitop3:0x7e
	v_mfma_f32_16x16x32_f16 v[22:25], a[152:155], v[86:89], v[22:25]
	v_bitop3_b32 v168, v168, v169, s18 bitop3:0xa8
	v_cmp_ne_u32_e32 vcc, 0, v168
	v_mfma_f32_16x16x32_f16 v[26:29], a[184:187], v[86:89], v[26:29]
	v_and_b32_e32 v90, v90, v167
	v_and_b32_e32 v91, v91, v167
	v_mfma_f32_16x16x32_f16 v[30:33], a[216:219], v[86:89], v[30:33]
	v_and_b32_e32 v92, v92, v167
	v_and_b32_e32 v93, v93, v167
	v_mfma_f32_16x16x32_f16 v[34:37], a[248:251], v[86:89], v[34:37]
	s_cbranch_vccnz .Lrestart7

.Lall_chunks_done:
	s_nop 1
	s_and_saveexec_b64 s[12:13], s[2:3]
	ds_write_b128 v174, v[6:9]
	ds_write_b128 v174, v[10:13] offset:512
	ds_write_b128 v174, v[14:17] offset:1024
	ds_write_b128 v174, v[18:21] offset:1536
	ds_write_b128 v174, v[22:25] offset:2048
	ds_write_b128 v174, v[26:29] offset:2560
	ds_write_b128 v174, v[30:33] offset:3072
	ds_write_b128 v174, v[34:37] offset:3584
	s_or_b64 exec, exec, s[12:13]
	v_cndmask_b32_e64 v6, v6, 0, s[2:3]
	v_cndmask_b32_e64 v7, v7, 0, s[2:3]
	v_cndmask_b32_e64 v8, v8, 0, s[2:3]
	v_cndmask_b32_e64 v9, v9, 0, s[2:3]
	v_cndmask_b32_e64 v10, v10, 0, s[2:3]
	v_cndmask_b32_e64 v11, v11, 0, s[2:3]
	v_cndmask_b32_e64 v12, v12, 0, s[2:3]
	v_cndmask_b32_e64 v13, v13, 0, s[2:3]
	v_cndmask_b32_e64 v14, v14, 0, s[2:3]
	v_cndmask_b32_e64 v15, v15, 0, s[2:3]
	v_cndmask_b32_e64 v16, v16, 0, s[2:3]
	v_cndmask_b32_e64 v17, v17, 0, s[2:3]
	global_load_dwordx4 v[46:49], v[4:5], off
	global_load_dwordx4 v[50:53], v[4:5], off offset:16
	global_load_dwordx4 v[38:41], v[4:5], off offset:128
	global_load_dwordx4 v[42:45], v[4:5], off offset:144
	s_cmp_lg_u32 s31, 0
	s_cbranch_scc1 .Lno_warm
	global_load_dwordx4 v[54:57], v[172:173], off
	global_load_dwordx4 v[58:61], v[172:173], off offset:1024
.Lno_warm:
	s_waitcnt lgkmcnt(0)
	s_barrier
	ds_read_b128 v[2:5], v175
	ds_read_b128 v[110:113], v175 offset:4096
	ds_read_b128 v[114:117], v175 offset:8192
	ds_read_b128 v[118:121], v175 offset:12288
	s_waitcnt lgkmcnt(0)
	v_pk_add_f32 v[4:5], v[4:5], v[112:113]
	v_pk_add_f32 v[2:3], v[2:3], v[110:111]
	v_pk_add_f32 v[4:5], v[4:5], v[116:117]
	v_pk_add_f32 v[2:3], v[2:3], v[114:115]
	v_pk_add_f32 v[4:5], v[4:5], v[120:121]
	v_pk_add_f32 v[2:3], v[2:3], v[118:119]
	v_add_f32_e32 v4, v4, v187
	v_add_f32_e32 v4, v4, v4
	v_add_f32_e32 v2, v2, v185
	v_mul_f32_e32 v4, 0x3fb8aa3b, v4
	v_mul_f32_e32 v2, 0xbfb8aa3b, v2
	v_exp_f32_e32 v4, v4
	v_add_f32_e32 v3, v3, v186
	v_exp_f32_e32 v2, v2
	v_mul_f32_e32 v3, 0xbfb8aa3b, v3
	v_exp_f32_e32 v3, v3
	v_add_f32_e32 v4, 1.0, v4
	v_add_f32_e32 v2, 1.0, v2
	v_rcp_f32_e32 v4, v4
	v_rcp_f32_e32 v2, v2
	v_add_f32_e32 v3, 1.0, v3
	v_rcp_f32_e32 v3, v3
	v_fma_f32 v4, v4, -2.0, 1.0
	v_mul_f32_e32 v2, v2, v4
	v_add_f32_e32 v5, v5, v188
	v_fmac_f32_e32 v2, v177, v3
	v_add_f32_e32 v3, v2, v2
	v_mul_f32_e32 v3, 0x3fb8aa3b, v3
	v_mul_f32_e32 v5, 0xbfb8aa3b, v5
	v_exp_f32_e32 v3, v3
	v_exp_f32_e32 v5, v5
	v_add_f32_e32 v3, 1.0, v3
	v_add_f32_e32 v4, 1.0, v5
	v_rcp_f32_e32 v3, v3
	v_rcp_f32_e32 v5, v4
	v_fma_f32 v3, v3, -2.0, 1.0
	v_mul_f32_e32 v4, v5, v3
	v_fma_mixlo_f16 v3, v5, v3, 0
	v_and_b32_e32 v3, 0xffffbfff, v3
	v_or_b32_sdwa v108, s34, v3 dst_sel:DWORD dst_unused:UNUSED_PAD src0_sel:DWORD src1_sel:WORD_0
	v_mov_b32_e32 v177, v2
	s_nop 0
	v_mov_b32_dpp v109, v108 row_ror:8 row_mask:0xf bank_mask:0xf
	v_mov_b32_dpp v5, v4 row_ror:8 row_mask:0xf bank_mask:0xf
	s_and_saveexec_b64 s[12:13], s[0:1]
	v_lshl_or_b32 v108, v109, 16, v108
	s_andn2_b64 vcc, exec, s[4:5]
	s_cbranch_vccnz .Lpub_sc1
	buffer_store_dword v108, v176, s[8:11], 0 offen

.Lrestart0:
	s_and_b64 vcc, exec, s[6:7]
	s_cbranch_vccnz .Lfast0
	s_add_i32 s17, s17, 1
	s_cmp_gt_u32 s17, 0x10000
	s_cselect_b64 s[6:7], -1, 0
	buffer_load_dwordx4 v[62:65], v166, s[8:11], s28 offen sc1
	buffer_load_dwordx4 v[66:69], v166, s[8:11], s28 offen offset:512 sc1
	buffer_load_dwordx4 v[70:73], v166, s[8:11], s28 offen offset:1024 sc1
	buffer_load_dwordx4 v[74:77], v166, s[8:11], s28 offen offset:1536 sc1
	buffer_load_dwordx4 v[78:81], v166, s[8:11], s28 offen offset:2048 sc1
	buffer_load_dwordx4 v[82:85], v166, s[8:11], s28 offen offset:2560 sc1
	buffer_load_dwordx4 v[86:89], v166, s[8:11], s28 offen offset:3072 sc1
	buffer_load_dwordx4 v[90:93], v166, s[8:11], s28 offen offset:3584 sc1
	s_waitcnt vmcnt(7)
	v_bitop3_b32 v168, v62, v63, s30 bitop3:0x7e
	v_bitop3_b32 v169, v64, v65, s30 bitop3:0x7e
	v_bitop3_b32 v168, v168, v169, s18 bitop3:0xa8
	v_cmp_ne_u32_e32 vcc, 0, v168
	s_cbranch_vccnz .Lrestart0
	v_and_b32_e32 v62, v62, v167
	v_and_b32_e32 v63, v63, v167
	v_and_b32_e32 v64, v64, v167
	v_and_b32_e32 v65, v65, v167
	s_nop 1
	s_branch .Lfast0
.Lrestart1:
	s_and_b64 vcc, exec, s[6:7]
	s_cbranch_vccnz .Lfast1
	s_add_i32 s17, s17, 1
	s_cmp_gt_u32 s17, 0x10000
	s_cselect_b64 s[6:7], -1, 0
	buffer_load_dwordx4 v[66:69], v166, s[8:11], s28 offen offset:512 sc1
	buffer_load_dwordx4 v[70:73], v166, s[8:11], s28 offen offset:1024 sc1
	buffer_load_dwordx4 v[74:77], v166, s[8:11], s28 offen offset:1536 sc1
	buffer_load_dwordx4 v[78:81], v166, s[8:11], s28 offen offset:2048 sc1
	buffer_load_dwordx4 v[82:85], v166, s[8:11], s28 offen offset:2560 sc1
	buffer_load_dwordx4 v[86:89], v166, s[8:11], s28 offen offset:3072 sc1
	buffer_load_dwordx4 v[90:93], v166, s[8:11], s28 offen offset:3584 sc1
	s_waitcnt vmcnt(6)
	v_bitop3_b32 v168, v66, v67, s30 bitop3:0x7e
	v_bitop3_b32 v169, v68, v69, s30 bitop3:0x7e
	v_bitop3_b32 v168, v168, v169, s18 bitop3:0xa8
	v_cmp_ne_u32_e32 vcc, 0, v168
	s_cbranch_vccnz .Lrestart1
	v_and_b32_e32 v66, v66, v167
	v_and_b32_e32 v67, v67, v167
	v_and_b32_e32 v68, v68, v167
	v_and_b32_e32 v69, v69, v167
	s_nop 1
	s_branch .Lfast1
.Lrestart2:
	s_and_b64 vcc, exec, s[6:7]
	s_cbranch_vccnz .Lfast2
	s_add_i32 s17, s17, 1
	s_cmp_gt_u32 s17, 0x10000
	s_cselect_b64 s[6:7], -1, 0
	buffer_load_dwordx4 v[70:73], v166, s[8:11], s28 offen offset:1024 sc1
	buffer_load_dwordx4 v[74:77], v166, s[8:11], s28 offen offset:1536 sc1
	buffer_load_dwordx4 v[78:81], v166, s[8:11], s28 offen offset:2048 sc1
	buffer_load_dwordx4 v[82:85], v166, s[8:11], s28 offen offset:2560 sc1
	buffer_load_dwordx4 v[86:89], v166, s[8:11], s28 offen offset:3072 sc1
	buffer_load_dwordx4 v[90:93], v166, s[8:11], s28 offen offset:3584 sc1
	s_waitcnt vmcnt(5)
	v_bitop3_b32 v168, v70, v71, s30 bitop3:0x7e
	v_bitop3_b32 v169, v72, v73, s30 bitop3:0x7e
	v_bitop3_b32 v168, v168, v169, s18 bitop3:0xa8
	v_cmp_ne_u32_e32 vcc, 0, v168
	s_cbranch_vccnz .Lrestart2
	v_and_b32_e32 v70, v70, v167
	v_and_b32_e32 v71, v71, v167
	v_and_b32_e32 v72, v72, v167
	v_and_b32_e32 v73, v73, v167
	s_nop 1
	s_branch .Lfast2
.Lrestart3:
	s_and_b64 vcc, exec, s[6:7]
	s_cbranch_vccnz .Lfast3
	s_add_i32 s17, s17, 1
	s_cmp_gt_u32 s17, 0x10000
	s_cselect_b64 s[6:7], -1, 0
	buffer_load_dwordx4 v[74:77], v166, s[8:11], s28 offen offset:1536 sc1
	buffer_load_dwordx4 v[78:81], v166, s[8:11], s28 offen offset:2048 sc1
	buffer_load_dwordx4 v[82:85], v166, s[8:11], s28 offen offset:2560 sc1
	buffer_load_dwordx4 v[86:89], v166, s[8:11], s28 offen offset:3072 sc1
	buffer_load_dwordx4 v[90:93], v166, s[8:11], s28 offen offset:3584 sc1
	s_waitcnt vmcnt(4)
	v_bitop3_b32 v168, v74, v75, s30 bitop3:0x7e
	v_bitop3_b32 v169, v76, v77, s30 bitop3:0x7e
	v_bitop3_b32 v168, v168, v169, s18 bitop3:0xa8
	v_cmp_ne_u32_e32 vcc, 0, v168
	s_cbranch_vccnz .Lrestart3
	v_and_b32_e32 v74, v74, v167
	v_and_b32_e32 v75, v75, v167
	v_and_b32_e32 v76, v76, v167
	v_and_b32_e32 v77, v77, v167
	s_nop 1
	s_branch .Lfast3
.Lrestart4:
	s_and_b64 vcc, exec, s[6:7]
	s_cbranch_vccnz .Lfast4
	s_add_i32 s17, s17, 1
	s_cmp_gt_u32 s17, 0x10000
	s_cselect_b64 s[6:7], -1, 0
	buffer_load_dwordx4 v[78:81], v166, s[8:11], s28 offen offset:2048 sc1
	buffer_load_dwordx4 v[82:85], v166, s[8:11], s28 offen offset:2560 sc1
	buffer_load_dwordx4 v[86:89], v166, s[8:11], s28 offen offset:3072 sc1
	buffer_load_dwordx4 v[90:93], v166, s[8:11], s28 offen offset:3584 sc1
	s_waitcnt vmcnt(3)
	v_bitop3_b32 v168, v78, v79, s30 bitop3:0x7e
	v_bitop3_b32 v169, v80, v81, s30 bitop3:0x7e
	v_bitop3_b32 v168, v168, v169, s18 bitop3:0xa8
	v_cmp_ne_u32_e32 vcc, 0, v168
	s_cbranch_vccnz .Lrestart4
	v_and_b32_e32 v78, v78, v167
	v_and_b32_e32 v79, v79, v167
	v_and_b32_e32 v80, v80, v167
	v_and_b32_e32 v81, v81, v167
	s_nop 1
	s_branch .Lfast4
.Lrestart5:
	s_and_b64 vcc, exec, s[6:7]
	s_cbranch_vccnz .Lfast5
	s_add_i32 s17, s17, 1
	s_cmp_gt_u32 s17, 0x10000
	s_cselect_b64 s[6:7], -1, 0
	buffer_load_dwordx4 v[82:85], v166, s[8:11], s28 offen offset:2560 sc1
	buffer_load_dwordx4 v[86:89], v166, s[8:11], s28 offen offset:3072 sc1
	buffer_load_dwordx4 v[90:93], v166, s[8:11], s28 offen offset:3584 sc1
	s_waitcnt vmcnt(2)
	v_bitop3_b32 v168, v82, v83, s30 bitop3:0x7e
	v_bitop3_b32 v169, v84, v85, s30 bitop3:0x7e
	v_bitop3_b32 v168, v168, v169, s18 bitop3:0xa8
	v_cmp_ne_u32_e32 vcc, 0, v168
	s_cbranch_vccnz .Lrestart5
	v_and_b32_e32 v82, v82, v167
	v_and_b32_e32 v83, v83, v167
	v_and_b32_e32 v84, v84, v167
	v_and_b32_e32 v85, v85, v167
	s_nop 1
	s_branch .Lfast5
.Lrestart6:
	s_and_b64 vcc, exec, s[6:7]
	s_cbranch_vccnz .Lfast6
	s_add_i32 s17, s17, 1
	s_cmp_gt_u32 s17, 0x10000
	s_cselect_b64 s[6:7], -1, 0
	buffer_load_dwordx4 v[86:89], v166, s[8:11], s28 offen offset:3072 sc1
	buffer_load_dwordx4 v[90:93], v166, s[8:11], s28 offen offset:3584 sc1
	s_waitcnt vmcnt(1)
	v_bitop3_b32 v168, v86, v87, s30 bitop3:0x7e
	v_bitop3_b32 v169, v88, v89, s30 bitop3:0x7e
	v_bitop3_b32 v168, v168, v169, s18 bitop3:0xa8
	v_cmp_ne_u32_e32 vcc, 0, v168
	s_cbranch_vccnz .Lrestart6
	v_and_b32_e32 v86, v86, v167
	v_and_b32_e32 v87, v87, v167
	v_and_b32_e32 v88, v88, v167
	v_and_b32_e32 v89, v89, v167
	s_nop 1
	s_branch .Lfast6
.Lrestart7:
	s_and_b64 vcc, exec, s[6:7]
	s_cbranch_vccnz .Lfast7
	s_add_i32 s17, s17, 1
	s_cmp_gt_u32 s17, 0x10000
	s_cselect_b64 s[6:7], -1, 0
	buffer_load_dwordx4 v[90:93], v166, s[8:11], s28 offen offset:3584 sc1
	s_waitcnt vmcnt(0)
	v_bitop3_b32 v168, v90, v91, s30 bitop3:0x7e
	v_bitop3_b32 v169, v92, v93, s30 bitop3:0x7e
	v_bitop3_b32 v168, v168, v169, s18 bitop3:0xa8
	v_cmp_ne_u32_e32 vcc, 0, v168
	s_cbranch_vccnz .Lrestart7
	v_and_b32_e32 v90, v90, v167
	v_and_b32_e32 v91, v91, v167
	v_and_b32_e32 v92, v92, v167
	v_and_b32_e32 v93, v93, v167
	s_nop 1
	s_branch .Lfast7
